# speedup vs baseline: 1.0934x; 1.0707x over previous
_Z11center_prepPKfPcPfS2_:
	s_load_dwordx2 s[6:7], s[0:1], 0x0
	s_load_dwordx4 s[8:11], s[0:1], 0x8
	s_load_dwordx2 s[12:13], s[0:1], 0x18
	v_lshrrev_b32_e32 v1, 3, v0
	v_and_b32_e32 v2, 7, v0
	v_lshlrev_b32_e32 v3, 10, v1
	v_lshl_or_b32 v136, v2, 4, v3
	v_mul_u32_u24_e32 v3, 0x110, v1
	v_lshl_add_u32 v137, v2, 4, v3
	v_and_b32_e32 v4, 31, v0
	v_lshrrev_b32_e32 v5, 5, v0
	v_mul_u32_u24_e32 v3, 0x110, v4
	v_lshl_add_u32 v138, v5, 5, v3
	v_lshlrev_b32_e32 v139, 5, v0
	v_lshlrev_b32_e32 v140, 2, v1
	v_mov_b32_e32 v142, -2.0
	v_mov_b32_e32 v143, -2.0
	s_lshl_b32 s14, s2, 15
	s_waitcnt lgkmcnt(0)
	s_add_u32 s16, s6, s14
	s_addc_u32 s17, s7, 0
	s_add_u32 s18, s16, 0x2000
	s_addc_u32 s19, s17, 0
	s_add_u32 s20, s16, 0x4000
	s_addc_u32 s21, s17, 0
	s_add_u32 s22, s16, 0x6000
	s_addc_u32 s23, s17, 0
	global_load_dwordx4 v[8:11], v136, s[16:17] offset:0 nt
	global_load_dwordx4 v[12:15], v136, s[16:17] offset:128 nt
	global_load_dwordx4 v[16:19], v136, s[16:17] offset:256 nt
	global_load_dwordx4 v[20:23], v136, s[16:17] offset:384 nt
	global_load_dwordx4 v[24:27], v136, s[16:17] offset:512 nt
	global_load_dwordx4 v[28:31], v136, s[16:17] offset:640 nt
	global_load_dwordx4 v[32:35], v136, s[16:17] offset:768 nt
	global_load_dwordx4 v[36:39], v136, s[16:17] offset:896 nt
	global_load_dwordx4 v[40:43], v136, s[18:19] offset:0 nt
	global_load_dwordx4 v[44:47], v136, s[18:19] offset:128 nt
	global_load_dwordx4 v[48:51], v136, s[18:19] offset:256 nt
	global_load_dwordx4 v[52:55], v136, s[18:19] offset:384 nt
	global_load_dwordx4 v[56:59], v136, s[18:19] offset:512 nt
	global_load_dwordx4 v[60:63], v136, s[18:19] offset:640 nt
	global_load_dwordx4 v[64:67], v136, s[18:19] offset:768 nt
	global_load_dwordx4 v[68:71], v136, s[18:19] offset:896 nt
	global_load_dwordx4 v[72:75], v136, s[20:21] offset:0 nt
	global_load_dwordx4 v[76:79], v136, s[20:21] offset:128 nt
	global_load_dwordx4 v[80:83], v136, s[20:21] offset:256 nt
	global_load_dwordx4 v[84:87], v136, s[20:21] offset:384 nt
	global_load_dwordx4 v[88:91], v136, s[20:21] offset:512 nt
	global_load_dwordx4 v[92:95], v136, s[20:21] offset:640 nt
	global_load_dwordx4 v[96:99], v136, s[20:21] offset:768 nt
	global_load_dwordx4 v[100:103], v136, s[20:21] offset:896 nt
	global_load_dwordx4 v[104:107], v136, s[22:23] offset:0 nt
	global_load_dwordx4 v[108:111], v136, s[22:23] offset:128 nt
	global_load_dwordx4 v[112:115], v136, s[22:23] offset:256 nt
	global_load_dwordx4 v[116:119], v136, s[22:23] offset:384 nt
	global_load_dwordx4 v[120:123], v136, s[22:23] offset:512 nt
	global_load_dwordx4 v[124:127], v136, s[22:23] offset:640 nt
	global_load_dwordx4 v[128:131], v136, s[22:23] offset:768 nt
	global_load_dwordx4 v[132:135], v136, s[22:23] offset:896 nt
	s_lshl_b32 s14, s2, 13
	s_add_u32 s24, s8, s14
	s_addc_u32 s25, s9, 0
	s_add_u32 s26, s24, 0x1000
	s_addc_u32 s27, s25, 0
	s_lshl_b32 s14, s2, 7
	s_add_u32 s28, s10, s14
	s_addc_u32 s29, s11, 0
	s_cmp_lg_u32 s2, 0
	s_cbranch_scc1 .Lprep_noinit
	v_cmp_gt_u32_e32 vcc, 16, v0
	s_and_saveexec_b64 s[30:31], vcc
	v_lshlrev_b32_e32 v1, 7, v0
	v_add_u32_e32 v1, 0x300000, v1
	v_mov_b32_e32 v2, 0
	v_mov_b32_e32 v3, 0
	global_store_dwordx2 v1, v[2:3], s[8:9]
	v_cmp_eq_u32_e32 vcc, 0, v0
	s_and_b64 exec, exec, vcc
	global_store_dword v2, v2, s[12:13]
	s_or_b64 exec, exec, s[30:31]
.Lprep_noinit:
	s_waitcnt vmcnt(31)
	v_pk_mul_f32 v[144:145], v[8:9], v[8:9]
	v_pk_fma_f32 v[144:145], v[10:11], v[10:11], v[144:145]
	v_pk_mul_f32 v[8:9], v[8:9], v[142:143]
	v_pk_mul_f32 v[10:11], v[10:11], v[142:143]
	v_cvt_pk_fp8_f32 v148, v8, v9
	s_nop 0
	v_cvt_pk_fp8_f32 v148, v10, v11 op_sel:[0,0,1]
	s_waitcnt vmcnt(30)
	v_pk_fma_f32 v[144:145], v[12:13], v[12:13], v[144:145]
	v_pk_fma_f32 v[144:145], v[14:15], v[14:15], v[144:145]
	v_pk_mul_f32 v[12:13], v[12:13], v[142:143]
	v_pk_mul_f32 v[14:15], v[14:15], v[142:143]
	v_cvt_pk_fp8_f32 v149, v12, v13
	s_nop 0
	v_cvt_pk_fp8_f32 v149, v14, v15 op_sel:[0,0,1]
	s_waitcnt vmcnt(29)
	v_pk_fma_f32 v[144:145], v[16:17], v[16:17], v[144:145]
	v_pk_fma_f32 v[144:145], v[18:19], v[18:19], v[144:145]
	v_pk_mul_f32 v[16:17], v[16:17], v[142:143]
	v_pk_mul_f32 v[18:19], v[18:19], v[142:143]
	v_cvt_pk_fp8_f32 v150, v16, v17
	s_nop 0
	v_cvt_pk_fp8_f32 v150, v18, v19 op_sel:[0,0,1]
	s_waitcnt vmcnt(28)
	v_pk_fma_f32 v[144:145], v[20:21], v[20:21], v[144:145]
	v_pk_fma_f32 v[144:145], v[22:23], v[22:23], v[144:145]
	v_pk_mul_f32 v[20:21], v[20:21], v[142:143]
	v_pk_mul_f32 v[22:23], v[22:23], v[142:143]
	v_cvt_pk_fp8_f32 v151, v20, v21
	s_nop 0
	v_cvt_pk_fp8_f32 v151, v22, v23 op_sel:[0,0,1]
	s_waitcnt vmcnt(27)
	v_pk_fma_f32 v[144:145], v[24:25], v[24:25], v[144:145]
	v_pk_fma_f32 v[144:145], v[26:27], v[26:27], v[144:145]
	v_pk_mul_f32 v[24:25], v[24:25], v[142:143]
	v_pk_mul_f32 v[26:27], v[26:27], v[142:143]
	v_cvt_pk_fp8_f32 v152, v24, v25
	s_nop 0
	v_cvt_pk_fp8_f32 v152, v26, v27 op_sel:[0,0,1]
	s_waitcnt vmcnt(26)
	v_pk_fma_f32 v[144:145], v[28:29], v[28:29], v[144:145]
	v_pk_fma_f32 v[144:145], v[30:31], v[30:31], v[144:145]
	v_pk_mul_f32 v[28:29], v[28:29], v[142:143]
	v_pk_mul_f32 v[30:31], v[30:31], v[142:143]
	v_cvt_pk_fp8_f32 v153, v28, v29
	s_nop 0
	v_cvt_pk_fp8_f32 v153, v30, v31 op_sel:[0,0,1]
	s_waitcnt vmcnt(25)
	v_pk_fma_f32 v[144:145], v[32:33], v[32:33], v[144:145]
	v_pk_fma_f32 v[144:145], v[34:35], v[34:35], v[144:145]
	v_pk_mul_f32 v[32:33], v[32:33], v[142:143]
	v_pk_mul_f32 v[34:35], v[34:35], v[142:143]
	v_cvt_pk_fp8_f32 v154, v32, v33
	s_nop 0
	v_cvt_pk_fp8_f32 v154, v34, v35 op_sel:[0,0,1]
	s_waitcnt vmcnt(24)
	v_pk_fma_f32 v[144:145], v[36:37], v[36:37], v[144:145]
	v_pk_fma_f32 v[144:145], v[38:39], v[38:39], v[144:145]
	v_pk_mul_f32 v[36:37], v[36:37], v[142:143]
	v_pk_mul_f32 v[38:39], v[38:39], v[142:143]
	v_cvt_pk_fp8_f32 v155, v36, v37
	s_nop 0
	v_cvt_pk_fp8_f32 v155, v38, v39 op_sel:[0,0,1]
	v_add_f32_e32 v160, v144, v145
	ds_write_b128 v137, v[148:151] offset:0
	ds_write_b128 v137, v[152:155] offset:128
	v_add_f32_dpp v161, v160, v160 quad_perm:[1,0,3,2] row_mask:0xf bank_mask:0xf
	s_nop 1
	v_add_f32_dpp v162, v161, v161 quad_perm:[2,3,0,1] row_mask:0xf bank_mask:0xf
	s_nop 1
	v_add_f32_dpp v156, v162, v162 row_half_mirror row_mask:0xf bank_mask:0xf
	s_waitcnt vmcnt(23)
	v_pk_mul_f32 v[144:145], v[40:41], v[40:41]
	v_pk_fma_f32 v[144:145], v[42:43], v[42:43], v[144:145]
	v_pk_mul_f32 v[40:41], v[40:41], v[142:143]
	v_pk_mul_f32 v[42:43], v[42:43], v[142:143]
	v_cvt_pk_fp8_f32 v148, v40, v41
	s_nop 0
	v_cvt_pk_fp8_f32 v148, v42, v43 op_sel:[0,0,1]
	s_waitcnt vmcnt(22)
	v_pk_fma_f32 v[144:145], v[44:45], v[44:45], v[144:145]
	v_pk_fma_f32 v[144:145], v[46:47], v[46:47], v[144:145]
	v_pk_mul_f32 v[44:45], v[44:45], v[142:143]
	v_pk_mul_f32 v[46:47], v[46:47], v[142:143]
	v_cvt_pk_fp8_f32 v149, v44, v45
	s_nop 0
	v_cvt_pk_fp8_f32 v149, v46, v47 op_sel:[0,0,1]
	s_waitcnt vmcnt(21)
	v_pk_fma_f32 v[144:145], v[48:49], v[48:49], v[144:145]
	v_pk_fma_f32 v[144:145], v[50:51], v[50:51], v[144:145]
	v_pk_mul_f32 v[48:49], v[48:49], v[142:143]
	v_pk_mul_f32 v[50:51], v[50:51], v[142:143]
	v_cvt_pk_fp8_f32 v150, v48, v49
	s_nop 0
	v_cvt_pk_fp8_f32 v150, v50, v51 op_sel:[0,0,1]
	s_waitcnt vmcnt(20)
	v_pk_fma_f32 v[144:145], v[52:53], v[52:53], v[144:145]
	v_pk_fma_f32 v[144:145], v[54:55], v[54:55], v[144:145]
	v_pk_mul_f32 v[52:53], v[52:53], v[142:143]
	v_pk_mul_f32 v[54:55], v[54:55], v[142:143]
	v_cvt_pk_fp8_f32 v151, v52, v53
	s_nop 0
	v_cvt_pk_fp8_f32 v151, v54, v55 op_sel:[0,0,1]
	s_waitcnt vmcnt(19)
	v_pk_fma_f32 v[144:145], v[56:57], v[56:57], v[144:145]
	v_pk_fma_f32 v[144:145], v[58:59], v[58:59], v[144:145]
	v_pk_mul_f32 v[56:57], v[56:57], v[142:143]
	v_pk_mul_f32 v[58:59], v[58:59], v[142:143]
	v_cvt_pk_fp8_f32 v152, v56, v57
	s_nop 0
	v_cvt_pk_fp8_f32 v152, v58, v59 op_sel:[0,0,1]
	s_waitcnt vmcnt(18)
	v_pk_fma_f32 v[144:145], v[60:61], v[60:61], v[144:145]
	v_pk_fma_f32 v[144:145], v[62:63], v[62:63], v[144:145]
	v_pk_mul_f32 v[60:61], v[60:61], v[142:143]
	v_pk_mul_f32 v[62:63], v[62:63], v[142:143]
	v_cvt_pk_fp8_f32 v153, v60, v61
	s_nop 0
	v_cvt_pk_fp8_f32 v153, v62, v63 op_sel:[0,0,1]
	s_waitcnt vmcnt(17)
	v_pk_fma_f32 v[144:145], v[64:65], v[64:65], v[144:145]
	v_pk_fma_f32 v[144:145], v[66:67], v[66:67], v[144:145]
	v_pk_mul_f32 v[64:65], v[64:65], v[142:143]
	v_pk_mul_f32 v[66:67], v[66:67], v[142:143]
	v_cvt_pk_fp8_f32 v154, v64, v65
	s_nop 0
	v_cvt_pk_fp8_f32 v154, v66, v67 op_sel:[0,0,1]
	s_waitcnt vmcnt(16)
	v_pk_fma_f32 v[144:145], v[68:69], v[68:69], v[144:145]
	v_pk_fma_f32 v[144:145], v[70:71], v[70:71], v[144:145]
	v_pk_mul_f32 v[68:69], v[68:69], v[142:143]
	v_pk_mul_f32 v[70:71], v[70:71], v[142:143]
	v_cvt_pk_fp8_f32 v155, v68, v69
	s_nop 0
	v_cvt_pk_fp8_f32 v155, v70, v71 op_sel:[0,0,1]
	v_add_f32_e32 v160, v144, v145
	ds_write_b128 v137, v[148:151] offset:2176
	ds_write_b128 v137, v[152:155] offset:2304
	v_add_f32_dpp v161, v160, v160 quad_perm:[1,0,3,2] row_mask:0xf bank_mask:0xf
	s_nop 1
	v_add_f32_dpp v162, v161, v161 quad_perm:[2,3,0,1] row_mask:0xf bank_mask:0xf
	s_nop 1
	v_add_f32_dpp v157, v162, v162 row_half_mirror row_mask:0xf bank_mask:0xf
	s_waitcnt vmcnt(15)
	v_pk_mul_f32 v[144:145], v[72:73], v[72:73]
	v_pk_fma_f32 v[144:145], v[74:75], v[74:75], v[144:145]
	v_pk_mul_f32 v[72:73], v[72:73], v[142:143]
	v_pk_mul_f32 v[74:75], v[74:75], v[142:143]
	v_cvt_pk_fp8_f32 v148, v72, v73
	s_nop 0
	v_cvt_pk_fp8_f32 v148, v74, v75 op_sel:[0,0,1]
	s_waitcnt vmcnt(14)
	v_pk_fma_f32 v[144:145], v[76:77], v[76:77], v[144:145]
	v_pk_fma_f32 v[144:145], v[78:79], v[78:79], v[144:145]
	v_pk_mul_f32 v[76:77], v[76:77], v[142:143]
	v_pk_mul_f32 v[78:79], v[78:79], v[142:143]
	v_cvt_pk_fp8_f32 v149, v76, v77
	s_nop 0
	v_cvt_pk_fp8_f32 v149, v78, v79 op_sel:[0,0,1]
	s_waitcnt vmcnt(13)
	v_pk_fma_f32 v[144:145], v[80:81], v[80:81], v[144:145]
	v_pk_fma_f32 v[144:145], v[82:83], v[82:83], v[144:145]
	v_pk_mul_f32 v[80:81], v[80:81], v[142:143]
	v_pk_mul_f32 v[82:83], v[82:83], v[142:143]
	v_cvt_pk_fp8_f32 v150, v80, v81
	s_nop 0
	v_cvt_pk_fp8_f32 v150, v82, v83 op_sel:[0,0,1]
	s_waitcnt vmcnt(12)
	v_pk_fma_f32 v[144:145], v[84:85], v[84:85], v[144:145]
	v_pk_fma_f32 v[144:145], v[86:87], v[86:87], v[144:145]
	v_pk_mul_f32 v[84:85], v[84:85], v[142:143]
	v_pk_mul_f32 v[86:87], v[86:87], v[142:143]
	v_cvt_pk_fp8_f32 v151, v84, v85
	s_nop 0
	v_cvt_pk_fp8_f32 v151, v86, v87 op_sel:[0,0,1]
	s_waitcnt vmcnt(11)
	v_pk_fma_f32 v[144:145], v[88:89], v[88:89], v[144:145]
	v_pk_fma_f32 v[144:145], v[90:91], v[90:91], v[144:145]
	v_pk_mul_f32 v[88:89], v[88:89], v[142:143]
	v_pk_mul_f32 v[90:91], v[90:91], v[142:143]
	v_cvt_pk_fp8_f32 v152, v88, v89
	s_nop 0
	v_cvt_pk_fp8_f32 v152, v90, v91 op_sel:[0,0,1]
	s_waitcnt vmcnt(10)
	v_pk_fma_f32 v[144:145], v[92:93], v[92:93], v[144:145]
	v_pk_fma_f32 v[144:145], v[94:95], v[94:95], v[144:145]
	v_pk_mul_f32 v[92:93], v[92:93], v[142:143]
	v_pk_mul_f32 v[94:95], v[94:95], v[142:143]
	v_cvt_pk_fp8_f32 v153, v92, v93
	s_nop 0
	v_cvt_pk_fp8_f32 v153, v94, v95 op_sel:[0,0,1]
	s_waitcnt vmcnt(9)
	v_pk_fma_f32 v[144:145], v[96:97], v[96:97], v[144:145]
	v_pk_fma_f32 v[144:145], v[98:99], v[98:99], v[144:145]
	v_pk_mul_f32 v[96:97], v[96:97], v[142:143]
	v_pk_mul_f32 v[98:99], v[98:99], v[142:143]
	v_cvt_pk_fp8_f32 v154, v96, v97
	s_nop 0
	v_cvt_pk_fp8_f32 v154, v98, v99 op_sel:[0,0,1]
	s_waitcnt vmcnt(8)
	v_pk_fma_f32 v[144:145], v[100:101], v[100:101], v[144:145]
	v_pk_fma_f32 v[144:145], v[102:103], v[102:103], v[144:145]
	v_pk_mul_f32 v[100:101], v[100:101], v[142:143]
	v_pk_mul_f32 v[102:103], v[102:103], v[142:143]
	v_cvt_pk_fp8_f32 v155, v100, v101
	s_nop 0
	v_cvt_pk_fp8_f32 v155, v102, v103 op_sel:[0,0,1]
	v_add_f32_e32 v160, v144, v145
	ds_write_b128 v137, v[148:151] offset:4352
	ds_write_b128 v137, v[152:155] offset:4480
	v_add_f32_dpp v161, v160, v160 quad_perm:[1,0,3,2] row_mask:0xf bank_mask:0xf
	s_nop 1
	v_add_f32_dpp v162, v161, v161 quad_perm:[2,3,0,1] row_mask:0xf bank_mask:0xf
	s_nop 1
	v_add_f32_dpp v158, v162, v162 row_half_mirror row_mask:0xf bank_mask:0xf
	s_waitcnt vmcnt(7)
	v_pk_mul_f32 v[144:145], v[104:105], v[104:105]
	v_pk_fma_f32 v[144:145], v[106:107], v[106:107], v[144:145]
	v_pk_mul_f32 v[104:105], v[104:105], v[142:143]
	v_pk_mul_f32 v[106:107], v[106:107], v[142:143]
	v_cvt_pk_fp8_f32 v148, v104, v105
	s_nop 0
	v_cvt_pk_fp8_f32 v148, v106, v107 op_sel:[0,0,1]
	s_waitcnt vmcnt(6)
	v_pk_fma_f32 v[144:145], v[108:109], v[108:109], v[144:145]
	v_pk_fma_f32 v[144:145], v[110:111], v[110:111], v[144:145]
	v_pk_mul_f32 v[108:109], v[108:109], v[142:143]
	v_pk_mul_f32 v[110:111], v[110:111], v[142:143]
	v_cvt_pk_fp8_f32 v149, v108, v109
	s_nop 0
	v_cvt_pk_fp8_f32 v149, v110, v111 op_sel:[0,0,1]
	s_waitcnt vmcnt(5)
	v_pk_fma_f32 v[144:145], v[112:113], v[112:113], v[144:145]
	v_pk_fma_f32 v[144:145], v[114:115], v[114:115], v[144:145]
	v_pk_mul_f32 v[112:113], v[112:113], v[142:143]
	v_pk_mul_f32 v[114:115], v[114:115], v[142:143]
	v_cvt_pk_fp8_f32 v150, v112, v113
	s_nop 0
	v_cvt_pk_fp8_f32 v150, v114, v115 op_sel:[0,0,1]
	s_waitcnt vmcnt(4)
	v_pk_fma_f32 v[144:145], v[116:117], v[116:117], v[144:145]
	v_pk_fma_f32 v[144:145], v[118:119], v[118:119], v[144:145]
	v_pk_mul_f32 v[116:117], v[116:117], v[142:143]
	v_pk_mul_f32 v[118:119], v[118:119], v[142:143]
	v_cvt_pk_fp8_f32 v151, v116, v117
	s_nop 0
	v_cvt_pk_fp8_f32 v151, v118, v119 op_sel:[0,0,1]
	s_waitcnt vmcnt(3)
	v_pk_fma_f32 v[144:145], v[120:121], v[120:121], v[144:145]
	v_pk_fma_f32 v[144:145], v[122:123], v[122:123], v[144:145]
	v_pk_mul_f32 v[120:121], v[120:121], v[142:143]
	v_pk_mul_f32 v[122:123], v[122:123], v[142:143]
	v_cvt_pk_fp8_f32 v152, v120, v121
	s_nop 0
	v_cvt_pk_fp8_f32 v152, v122, v123 op_sel:[0,0,1]
	s_waitcnt vmcnt(2)
	v_pk_fma_f32 v[144:145], v[124:125], v[124:125], v[144:145]
	v_pk_fma_f32 v[144:145], v[126:127], v[126:127], v[144:145]
	v_pk_mul_f32 v[124:125], v[124:125], v[142:143]
	v_pk_mul_f32 v[126:127], v[126:127], v[142:143]
	v_cvt_pk_fp8_f32 v153, v124, v125
	s_nop 0
	v_cvt_pk_fp8_f32 v153, v126, v127 op_sel:[0,0,1]
	s_waitcnt vmcnt(1)
	v_pk_fma_f32 v[144:145], v[128:129], v[128:129], v[144:145]
	v_pk_fma_f32 v[144:145], v[130:131], v[130:131], v[144:145]
	v_pk_mul_f32 v[128:129], v[128:129], v[142:143]
	v_pk_mul_f32 v[130:131], v[130:131], v[142:143]
	v_cvt_pk_fp8_f32 v154, v128, v129
	s_nop 0
	v_cvt_pk_fp8_f32 v154, v130, v131 op_sel:[0,0,1]
	s_waitcnt vmcnt(0)
	v_pk_fma_f32 v[144:145], v[132:133], v[132:133], v[144:145]
	v_pk_fma_f32 v[144:145], v[134:135], v[134:135], v[144:145]
	v_pk_mul_f32 v[132:133], v[132:133], v[142:143]
	v_pk_mul_f32 v[134:135], v[134:135], v[142:143]
	v_cvt_pk_fp8_f32 v155, v132, v133
	s_nop 0
	v_cvt_pk_fp8_f32 v155, v134, v135 op_sel:[0,0,1]
	v_add_f32_e32 v160, v144, v145
	ds_write_b128 v137, v[148:151] offset:6528
	ds_write_b128 v137, v[152:155] offset:6656
	v_add_f32_dpp v161, v160, v160 quad_perm:[1,0,3,2] row_mask:0xf bank_mask:0xf
	s_nop 1
	v_add_f32_dpp v162, v161, v161 quad_perm:[2,3,0,1] row_mask:0xf bank_mask:0xf
	s_nop 1
	v_add_f32_dpp v159, v162, v162 row_half_mirror row_mask:0xf bank_mask:0xf
	v_and_b32_e32 v2, 7, v0
	v_cmp_eq_u32_e32 vcc, 0, v2
	s_and_saveexec_b64 s[30:31], vcc
	global_store_dword v140, v156, s[28:29] offset:0
	global_store_dword v140, v157, s[28:29] offset:32
	global_store_dword v140, v158, s[28:29] offset:64
	global_store_dword v140, v159, s[28:29] offset:96
	s_or_b64 exec, exec, s[30:31]
	s_waitcnt lgkmcnt(0)
	ds_read_b128 v[8:11], v138 offset:0
	ds_read_b128 v[12:15], v138 offset:16
	ds_read_b128 v[16:19], v138 offset:64
	ds_read_b128 v[20:23], v138 offset:80
	ds_read_b128 v[24:27], v138 offset:128
	ds_read_b128 v[28:31], v138 offset:144
	ds_read_b128 v[32:35], v138 offset:192
	ds_read_b128 v[36:39], v138 offset:208
	s_waitcnt lgkmcnt(6)
	global_store_dwordx4 v139, v[8:11], s[24:25] offset:0
	global_store_dwordx4 v139, v[12:15], s[24:25] offset:16
	s_waitcnt lgkmcnt(4)
	global_store_dwordx4 v139, v[16:19], s[24:25] offset:2048
	global_store_dwordx4 v139, v[20:23], s[24:25] offset:2064
	s_waitcnt lgkmcnt(2)
	global_store_dwordx4 v139, v[24:27], s[26:27] offset:0
	global_store_dwordx4 v139, v[28:31], s[26:27] offset:16
	s_waitcnt lgkmcnt(0)
	global_store_dwordx4 v139, v[32:35], s[26:27] offset:2048
	global_store_dwordx4 v139, v[36:39], s[26:27] offset:2064
	s_endpgm

	.amdhsa_kernel _Z11center_prepPKfPcPfS2_
		.amdhsa_group_segment_fixed_size 8704
		.amdhsa_private_segment_fixed_size 0
		.amdhsa_kernarg_size 32
		.amdhsa_user_sgpr_count 2
		.amdhsa_user_sgpr_dispatch_ptr 0
		.amdhsa_user_sgpr_queue_ptr 0
		.amdhsa_user_sgpr_kernarg_segment_ptr 1
		.amdhsa_user_sgpr_dispatch_id 0
		.amdhsa_user_sgpr_kernarg_preload_length 0
		.amdhsa_user_sgpr_kernarg_preload_offset 0
		.amdhsa_user_sgpr_private_segment_size 0
		.amdhsa_uses_dynamic_stack 0
		.amdhsa_enable_private_segment 0
		.amdhsa_system_sgpr_workgroup_id_x 1
		.amdhsa_system_sgpr_workgroup_id_y 0
		.amdhsa_system_sgpr_workgroup_id_z 0
		.amdhsa_system_sgpr_workgroup_info 0
		.amdhsa_system_vgpr_workitem_id 0
		.amdhsa_next_free_vgpr 164
		.amdhsa_next_free_sgpr 96
		.amdhsa_accum_offset 164
		.amdhsa_reserve_vcc 1
		.amdhsa_float_round_mode_32 0
		.amdhsa_float_round_mode_16_64 0
		.amdhsa_float_denorm_mode_32 3
		.amdhsa_float_denorm_mode_16_64 3
		.amdhsa_dx10_clamp 1
		.amdhsa_ieee_mode 1
		.amdhsa_fp16_overflow 0
		.amdhsa_tg_split 0
		.amdhsa_exception_fp_ieee_invalid_op 0
		.amdhsa_exception_fp_denorm_src 0
		.amdhsa_exception_fp_ieee_div_zero 0
		.amdhsa_exception_fp_ieee_overflow 0
		.amdhsa_exception_fp_ieee_underflow 0
		.amdhsa_exception_fp_ieee_inexact 0
		.amdhsa_exception_int_div_zero 0
	.end_amdhsa_kernel

.Lfunc_end0:
	.size	_Z11center_prepPKfPcPfS2_, .Lfunc_end0-_Z11center_prepPKfPcPfS2_
	.set _Z11center_prepPKfPcPfS2_.num_vgpr, 164
	.set _Z11center_prepPKfPcPfS2_.num_agpr, 0
	.set _Z11center_prepPKfPcPfS2_.numbered_sgpr, 12
	.set _Z11center_prepPKfPcPfS2_.num_named_barrier, 0
	.set _Z11center_prepPKfPcPfS2_.private_seg_size, 0
	.set _Z11center_prepPKfPcPfS2_.uses_vcc, 1
	.set _Z11center_prepPKfPcPfS2_.uses_flat_scratch, 0
	.set _Z11center_prepPKfPcPfS2_.has_dyn_sized_stack, 0
	.set _Z11center_prepPKfPcPfS2_.has_recursion, 0
	.set _Z11center_prepPKfPcPfS2_.has_indirect_call, 0

_Z11center_mainPKfPKcS0_Pf:
	s_load_dwordx4 s[4:7], s[0:1], 0x0
	s_load_dwordx2 s[8:9], s[0:1], 0x10
	s_and_b32 s3, s2, 7
	s_lshr_b32 s12, s2, 3
	s_mov_b32 s30, s2
	v_lshrrev_b32_e32 v1, 6, v0
	v_and_b32_e32 v2, 63, v0
	v_bfe_u32 v3, v0, 3, 3
	v_and_b32_e32 v4, 7, v0
	v_lshrrev_b32_e32 v5, 7, v0
	v_bfe_u32 v6, v0, 6, 1
	v_lshl_or_b32 v7, v5, 3, v3
	v_lshlrev_b32_e32 v8, 10, v7
	v_lshl_or_b32 v8, v6, 9, v8
	v_lshl_or_b32 v242, v4, 4, v8
	v_lshlrev_b32_e32 v17, 15, v1
	v_lshl_or_b32 v243, v2, 5, v17
	v_lshlrev_b32_e32 v254, 3, v0
	s_lshl_b32 s13, s3, 22
	s_lshl_b32 s14, s12, 15
	s_add_u32 s13, s13, s14
	s_lshl_b32 s15, s3, 18
	s_lshl_b32 s28, s3, 12
	s_waitcnt lgkmcnt(0)
	s_add_u32 s16, s4, s13
	s_addc_u32 s17, s5, 0
	s_add_u32 s18, s16, 0x100000
	s_addc_u32 s19, s17, 0
	s_add_u32 s20, s16, 0x200000
	s_addc_u32 s21, s17, 0
	s_add_u32 s22, s16, 0x300000
	s_addc_u32 s23, s17, 0
	s_add_u32 s24, s6, s15
	s_addc_u32 s25, s7, 0
	s_add_u32 s8, s8, s28
	s_addc_u32 s9, s9, 0
	s_add_u32 s32, s24, 0x1000
	s_addc_u32 s33, s25, 0
	s_add_u32 s34, s24, 0x2000
	s_addc_u32 s35, s25, 0
	s_add_u32 s36, s24, 0x3000
	s_addc_u32 s37, s25, 0
	s_add_u32 s38, s24, 0x4000
	s_addc_u32 s39, s25, 0
	s_add_u32 s40, s24, 0x5000
	s_addc_u32 s41, s25, 0
	s_add_u32 s42, s24, 0x6000
	s_addc_u32 s43, s25, 0
	s_add_u32 s44, s24, 0x7000
	s_addc_u32 s45, s25, 0
	global_load_dwordx2 v[252:253], v254, s[8:9]
	global_load_dwordx4 v[146:149], v242, s[16:17] offset:0 nt
	global_load_dwordx4 v[150:153], v242, s[16:17] offset:128 nt
	global_load_dwordx4 v[154:157], v242, s[16:17] offset:256 nt
	global_load_dwordx4 v[158:161], v242, s[16:17] offset:384 nt
	global_load_dwordx4 v[34:37], v243, s[24:25] offset:0
	global_load_dwordx4 v[38:41], v243, s[24:25] offset:16
	global_load_dwordx4 v[26:29], v243, s[24:25] offset:2048
	global_load_dwordx4 v[30:33], v243, s[24:25] offset:2064
	global_load_dwordx4 v[50:53], v243, s[32:33] offset:0
	global_load_dwordx4 v[54:57], v243, s[32:33] offset:16
	global_load_dwordx4 v[42:45], v243, s[32:33] offset:2048
	global_load_dwordx4 v[46:49], v243, s[32:33] offset:2064
	global_load_dwordx4 v[18:21], v243, s[34:35] offset:0
	global_load_dwordx4 v[22:25], v243, s[34:35] offset:16
	global_load_dwordx4 v[130:133], v243, s[34:35] offset:2048
	global_load_dwordx4 v[134:137], v243, s[34:35] offset:2064
	global_load_dwordx4 v[122:125], v243, s[36:37] offset:0
	global_load_dwordx4 v[126:129], v243, s[36:37] offset:16
	global_load_dwordx4 v[138:141], v243, s[36:37] offset:2048
	global_load_dwordx4 v[142:145], v243, s[36:37] offset:2064
	global_load_dwordx4 v[98:101], v243, s[38:39] offset:0
	global_load_dwordx4 v[102:105], v243, s[38:39] offset:16
	global_load_dwordx4 v[90:93], v243, s[38:39] offset:2048
	global_load_dwordx4 v[94:97], v243, s[38:39] offset:2064
	global_load_dwordx4 v[114:117], v243, s[40:41] offset:0
	global_load_dwordx4 v[118:121], v243, s[40:41] offset:16
	global_load_dwordx4 v[106:109], v243, s[40:41] offset:2048
	global_load_dwordx4 v[110:113], v243, s[40:41] offset:2064
	global_load_dwordx4 v[58:61], v243, s[42:43] offset:0
	global_load_dwordx4 v[62:65], v243, s[42:43] offset:16
	global_load_dwordx4 v[66:69], v243, s[42:43] offset:2048
	global_load_dwordx4 v[70:73], v243, s[42:43] offset:2064
	global_load_dwordx4 v[74:77], v243, s[44:45] offset:0
	global_load_dwordx4 v[78:81], v243, s[44:45] offset:16
	global_load_dwordx4 v[82:85], v243, s[44:45] offset:2048
	global_load_dwordx4 v[86:89], v243, s[44:45] offset:2064
	v_mul_u32_u24_e32 v9, 0x110, v7
	v_lshl_add_u32 v9, v6, 7, v9
	v_lshl_add_u32 v244, v4, 4, v9
	v_lshlrev_b32_e32 v10, 6, v7
	v_lshl_or_b32 v10, v6, 5, v10
	v_lshl_or_b32 v245, v4, 2, v10
	v_and_b32_e32 v11, 31, v0
	v_bfe_u32 v12, v0, 5, 1
	v_mul_u32_u24_e32 v13, 0x110, v11
	v_lshl_add_u32 v246, v12, 5, v13
	v_lshlrev_b32_e32 v14, 9, v1
	v_lshl_or_b32 v247, v12, 4, v14
	v_xor_b32_e32 v15, 32, v2
	v_lshlrev_b32_e32 v248, 2, v15
	v_lshlrev_b32_e32 v16, 7, v1
	v_lshl_or_b32 v249, v11, 2, v16
	v_mov_b32_e32 v250, 0x7f7f7f7f
	s_waitcnt vmcnt(32)
	ds_write_b64 v254, v[252:253] offset:34816
	v_mul_f32_e32 v6, v146, v146
	v_mul_f32_e32 v7, v150, v150
	v_cvt_pk_fp8_f32 v2, v146, v147
	v_cvt_pk_fp8_f32 v3, v150, v151
	v_cvt_pk_fp8_f32 v4, v154, v155
	v_cvt_pk_fp8_f32 v5, v158, v159
	v_fmac_f32_e32 v6, v147, v147
	v_fmac_f32_e32 v7, v151, v151
	v_fmac_f32_e32 v6, v148, v148
	v_fmac_f32_e32 v7, v152, v152
	v_fmac_f32_e32 v6, v149, v149
	v_fmac_f32_e32 v7, v153, v153
	v_fmac_f32_e32 v6, v154, v154
	v_fmac_f32_e32 v7, v158, v158
	v_fmac_f32_e32 v6, v155, v155
	v_fmac_f32_e32 v7, v159, v159
	v_fmac_f32_e32 v6, v156, v156
	v_fmac_f32_e32 v7, v160, v160
	v_fmac_f32_e32 v6, v157, v157
	v_fmac_f32_e32 v7, v161, v161
	v_cvt_pk_fp8_f32 v2, v148, v149 op_sel:[0,0,1]
	v_cvt_pk_fp8_f32 v3, v152, v153 op_sel:[0,0,1]
	v_cvt_pk_fp8_f32 v4, v156, v157 op_sel:[0,0,1]
	v_cvt_pk_fp8_f32 v5, v160, v161 op_sel:[0,0,1]
	v_add_f32_e32 v6, v6, v7
	s_nop 0
	ds_write_b128 v244, v[2:5] offset:0
	ds_write_b32 v245, v6 offset:38912
	global_load_dwordx4 v[162:165], v242, s[18:19] offset:0 nt
	global_load_dwordx4 v[166:169], v242, s[18:19] offset:128 nt
	global_load_dwordx4 v[170:173], v242, s[18:19] offset:256 nt
	global_load_dwordx4 v[174:177], v242, s[18:19] offset:384 nt
	s_waitcnt lgkmcnt(0)
	s_barrier
	ds_read_b128 v[210:213], v246 offset:0
	ds_read_b128 v[214:217], v246 offset:16
	ds_read_b128 v[2:5], v247 offset:34816
	ds_read_b128 v[6:9], v247 offset:34848
	ds_read_b128 v[10:13], v247 offset:34880
	ds_read_b128 v[14:17], v247 offset:34912
	ds_read_b128 v[218:221], v246 offset:64
	ds_read_b128 v[222:225], v246 offset:80
	ds_read_b128 v[226:229], v246 offset:128
	ds_read_b128 v[230:233], v246 offset:144
	ds_read_b128 v[234:237], v246 offset:192
	ds_read_b128 v[238:241], v246 offset:208
	s_waitcnt vmcnt(34) lgkmcnt(6)
	v_mfma_scale_f32_32x32x64_f8f6f4 v[2:17], v[34:41], v[210:217], v[2:17], v250, v250 op_sel_hi:[0,0,0]
	s_waitcnt vmcnt(32) lgkmcnt(4)
	v_mfma_scale_f32_32x32x64_f8f6f4 v[2:17], v[26:33], v[218:225], v[2:17], v250, v250 op_sel_hi:[0,0,0]
	s_waitcnt vmcnt(30) lgkmcnt(2)
	v_mfma_scale_f32_32x32x64_f8f6f4 v[2:17], v[50:57], v[226:233], v[2:17], v250, v250 op_sel_hi:[0,0,0]
	s_waitcnt vmcnt(28) lgkmcnt(0)
	v_mfma_scale_f32_32x32x64_f8f6f4 v[2:17], v[42:49], v[234:241], v[2:17], v250, v250 op_sel_hi:[0,0,0]
	s_nop 15
	s_nop 3
	v_min3_f32 v2, v2, v3, v4
	v_min3_f32 v5, v5, v6, v7
	v_min3_f32 v8, v8, v9, v10
	v_min3_f32 v11, v11, v12, v13
	v_min3_f32 v14, v14, v15, v16
	v_min3_f32 v2, v2, v5, v8
	v_min3_f32 v11, v11, v14, v17
	v_min_f32_e32 v251, v2, v11
	ds_read_b128 v[2:5], v247 offset:34944
	ds_read_b128 v[6:9], v247 offset:34976
	ds_read_b128 v[10:13], v247 offset:35008
	ds_read_b128 v[14:17], v247 offset:35040
	s_waitcnt vmcnt(26) lgkmcnt(0)
	v_mfma_scale_f32_32x32x64_f8f6f4 v[2:17], v[18:25], v[210:217], v[2:17], v250, v250 op_sel_hi:[0,0,0]
	s_waitcnt vmcnt(24)
	v_mfma_scale_f32_32x32x64_f8f6f4 v[2:17], v[130:137], v[218:225], v[2:17], v250, v250 op_sel_hi:[0,0,0]
	s_waitcnt vmcnt(22)
	v_mfma_scale_f32_32x32x64_f8f6f4 v[2:17], v[122:129], v[226:233], v[2:17], v250, v250 op_sel_hi:[0,0,0]
	s_waitcnt vmcnt(20)
	v_mfma_scale_f32_32x32x64_f8f6f4 v[2:17], v[138:145], v[234:241], v[2:17], v250, v250 op_sel_hi:[0,0,0]
	s_nop 15
	s_nop 3
	v_min3_f32 v2, v2, v3, v4
	v_min3_f32 v5, v5, v6, v7
	v_min3_f32 v8, v8, v9, v10
	v_min3_f32 v11, v11, v12, v13
	v_min3_f32 v14, v14, v15, v16
	v_min3_f32 v2, v2, v5, v8
	v_min3_f32 v11, v11, v14, v17
	v_min3_f32 v251, v251, v2, v11
	ds_read_b128 v[2:5], v247 offset:35072
	ds_read_b128 v[6:9], v247 offset:35104
	ds_read_b128 v[10:13], v247 offset:35136
	ds_read_b128 v[14:17], v247 offset:35168
	s_waitcnt vmcnt(18) lgkmcnt(0)
	v_mfma_scale_f32_32x32x64_f8f6f4 v[2:17], v[98:105], v[210:217], v[2:17], v250, v250 op_sel_hi:[0,0,0]
	s_waitcnt vmcnt(16)
	v_mfma_scale_f32_32x32x64_f8f6f4 v[2:17], v[90:97], v[218:225], v[2:17], v250, v250 op_sel_hi:[0,0,0]
	s_waitcnt vmcnt(14)
	v_mfma_scale_f32_32x32x64_f8f6f4 v[2:17], v[114:121], v[226:233], v[2:17], v250, v250 op_sel_hi:[0,0,0]
	s_waitcnt vmcnt(12)
	v_mfma_scale_f32_32x32x64_f8f6f4 v[2:17], v[106:113], v[234:241], v[2:17], v250, v250 op_sel_hi:[0,0,0]
	s_nop 15
	s_nop 3
	v_min3_f32 v2, v2, v3, v4
	v_min3_f32 v5, v5, v6, v7
	v_min3_f32 v8, v8, v9, v10
	v_min3_f32 v11, v11, v12, v13
	v_min3_f32 v14, v14, v15, v16
	v_min3_f32 v2, v2, v5, v8
	v_min3_f32 v11, v11, v14, v17
	v_min3_f32 v251, v251, v2, v11
	ds_read_b128 v[2:5], v247 offset:35200
	ds_read_b128 v[6:9], v247 offset:35232
	ds_read_b128 v[10:13], v247 offset:35264
	ds_read_b128 v[14:17], v247 offset:35296
	s_waitcnt vmcnt(10) lgkmcnt(0)
	v_mfma_scale_f32_32x32x64_f8f6f4 v[2:17], v[58:65], v[210:217], v[2:17], v250, v250 op_sel_hi:[0,0,0]
	s_waitcnt vmcnt(8)
	v_mfma_scale_f32_32x32x64_f8f6f4 v[2:17], v[66:73], v[218:225], v[2:17], v250, v250 op_sel_hi:[0,0,0]
	s_waitcnt vmcnt(6)
	v_mfma_scale_f32_32x32x64_f8f6f4 v[2:17], v[74:81], v[226:233], v[2:17], v250, v250 op_sel_hi:[0,0,0]
	s_waitcnt vmcnt(4)
	v_mfma_scale_f32_32x32x64_f8f6f4 v[2:17], v[82:89], v[234:241], v[2:17], v250, v250 op_sel_hi:[0,0,0]
	s_nop 15
	s_nop 3
	v_min3_f32 v2, v2, v3, v4
	v_min3_f32 v5, v5, v6, v7
	v_min3_f32 v8, v8, v9, v10
	v_min3_f32 v11, v11, v12, v13
	v_min3_f32 v14, v14, v15, v16
	v_min3_f32 v2, v2, v5, v8
	v_min3_f32 v11, v11, v14, v17
	v_min3_f32 v251, v251, v2, v11
	ds_bpermute_b32 v3, v248, v251
	s_waitcnt lgkmcnt(0)
	v_min_f32_e32 v2, v251, v3
	ds_write_b32 v249, v2 offset:47104
	global_load_dwordx4 v[178:181], v242, s[20:21] offset:0 nt
	global_load_dwordx4 v[182:185], v242, s[20:21] offset:128 nt
	global_load_dwordx4 v[186:189], v242, s[20:21] offset:256 nt
	global_load_dwordx4 v[190:193], v242, s[20:21] offset:384 nt
	s_waitcnt vmcnt(4)
	v_mul_f32_e32 v6, v162, v162
	v_mul_f32_e32 v7, v166, v166
	v_cvt_pk_fp8_f32 v2, v162, v163
	v_cvt_pk_fp8_f32 v3, v166, v167
	v_cvt_pk_fp8_f32 v4, v170, v171
	v_cvt_pk_fp8_f32 v5, v174, v175
	v_fmac_f32_e32 v6, v163, v163
	v_fmac_f32_e32 v7, v167, v167
	v_fmac_f32_e32 v6, v164, v164
	v_fmac_f32_e32 v7, v168, v168
	v_fmac_f32_e32 v6, v165, v165
	v_fmac_f32_e32 v7, v169, v169
	v_fmac_f32_e32 v6, v170, v170
	v_fmac_f32_e32 v7, v174, v174
	v_fmac_f32_e32 v6, v171, v171
	v_fmac_f32_e32 v7, v175, v175
	v_fmac_f32_e32 v6, v172, v172
	v_fmac_f32_e32 v7, v176, v176
	v_fmac_f32_e32 v6, v173, v173
	v_fmac_f32_e32 v7, v177, v177
	v_cvt_pk_fp8_f32 v2, v164, v165 op_sel:[0,0,1]
	v_cvt_pk_fp8_f32 v3, v168, v169 op_sel:[0,0,1]
	v_cvt_pk_fp8_f32 v4, v172, v173 op_sel:[0,0,1]
	v_cvt_pk_fp8_f32 v5, v176, v177 op_sel:[0,0,1]
	v_add_f32_e32 v6, v6, v7
	s_nop 0
	ds_write_b128 v244, v[2:5] offset:8704
	ds_write_b32 v245, v6 offset:40960
	s_waitcnt lgkmcnt(0)
	s_barrier
	ds_read_b128 v[210:213], v246 offset:8704
	ds_read_b128 v[214:217], v246 offset:8720
	ds_read_b128 v[2:5], v247 offset:34816
	ds_read_b128 v[6:9], v247 offset:34848
	ds_read_b128 v[10:13], v247 offset:34880
	ds_read_b128 v[14:17], v247 offset:34912
	ds_read_b128 v[218:221], v246 offset:8768
	ds_read_b128 v[222:225], v246 offset:8784
	ds_read_b128 v[226:229], v246 offset:8832
	ds_read_b128 v[230:233], v246 offset:8848
	ds_read_b128 v[234:237], v246 offset:8896
	ds_read_b128 v[238:241], v246 offset:8912
	s_waitcnt lgkmcnt(6)
	v_mfma_scale_f32_32x32x64_f8f6f4 v[2:17], v[34:41], v[210:217], v[2:17], v250, v250 op_sel_hi:[0,0,0]
	s_waitcnt lgkmcnt(4)
	v_mfma_scale_f32_32x32x64_f8f6f4 v[2:17], v[26:33], v[218:225], v[2:17], v250, v250 op_sel_hi:[0,0,0]
	s_waitcnt lgkmcnt(2)
	v_mfma_scale_f32_32x32x64_f8f6f4 v[2:17], v[50:57], v[226:233], v[2:17], v250, v250 op_sel_hi:[0,0,0]
	s_waitcnt lgkmcnt(0)
	v_mfma_scale_f32_32x32x64_f8f6f4 v[2:17], v[42:49], v[234:241], v[2:17], v250, v250 op_sel_hi:[0,0,0]
	s_nop 15
	s_nop 3
	v_min3_f32 v2, v2, v3, v4
	v_min3_f32 v5, v5, v6, v7
	v_min3_f32 v8, v8, v9, v10
	v_min3_f32 v11, v11, v12, v13
	v_min3_f32 v14, v14, v15, v16
	v_min3_f32 v2, v2, v5, v8
	v_min3_f32 v11, v11, v14, v17
	v_min_f32_e32 v251, v2, v11
	ds_read_b128 v[2:5], v247 offset:34944
	ds_read_b128 v[6:9], v247 offset:34976
	ds_read_b128 v[10:13], v247 offset:35008
	ds_read_b128 v[14:17], v247 offset:35040
	s_waitcnt lgkmcnt(0)
	v_mfma_scale_f32_32x32x64_f8f6f4 v[2:17], v[18:25], v[210:217], v[2:17], v250, v250 op_sel_hi:[0,0,0]
	v_mfma_scale_f32_32x32x64_f8f6f4 v[2:17], v[130:137], v[218:225], v[2:17], v250, v250 op_sel_hi:[0,0,0]
	v_mfma_scale_f32_32x32x64_f8f6f4 v[2:17], v[122:129], v[226:233], v[2:17], v250, v250 op_sel_hi:[0,0,0]
	v_mfma_scale_f32_32x32x64_f8f6f4 v[2:17], v[138:145], v[234:241], v[2:17], v250, v250 op_sel_hi:[0,0,0]
	s_nop 15
	s_nop 3
	v_min3_f32 v2, v2, v3, v4
	v_min3_f32 v5, v5, v6, v7
	v_min3_f32 v8, v8, v9, v10
	v_min3_f32 v11, v11, v12, v13
	v_min3_f32 v14, v14, v15, v16
	v_min3_f32 v2, v2, v5, v8
	v_min3_f32 v11, v11, v14, v17
	v_min3_f32 v251, v251, v2, v11
	ds_read_b128 v[2:5], v247 offset:35072
	ds_read_b128 v[6:9], v247 offset:35104
	ds_read_b128 v[10:13], v247 offset:35136
	ds_read_b128 v[14:17], v247 offset:35168
	s_waitcnt lgkmcnt(0)
	v_mfma_scale_f32_32x32x64_f8f6f4 v[2:17], v[98:105], v[210:217], v[2:17], v250, v250 op_sel_hi:[0,0,0]
	v_mfma_scale_f32_32x32x64_f8f6f4 v[2:17], v[90:97], v[218:225], v[2:17], v250, v250 op_sel_hi:[0,0,0]
	v_mfma_scale_f32_32x32x64_f8f6f4 v[2:17], v[114:121], v[226:233], v[2:17], v250, v250 op_sel_hi:[0,0,0]
	v_mfma_scale_f32_32x32x64_f8f6f4 v[2:17], v[106:113], v[234:241], v[2:17], v250, v250 op_sel_hi:[0,0,0]
	s_nop 15
	s_nop 3
	v_min3_f32 v2, v2, v3, v4
	v_min3_f32 v5, v5, v6, v7
	v_min3_f32 v8, v8, v9, v10
	v_min3_f32 v11, v11, v12, v13
	v_min3_f32 v14, v14, v15, v16
	v_min3_f32 v2, v2, v5, v8
	v_min3_f32 v11, v11, v14, v17
	v_min3_f32 v251, v251, v2, v11
	ds_read_b128 v[2:5], v247 offset:35200
	ds_read_b128 v[6:9], v247 offset:35232
	ds_read_b128 v[10:13], v247 offset:35264
	ds_read_b128 v[14:17], v247 offset:35296
	s_waitcnt lgkmcnt(0)
	v_mfma_scale_f32_32x32x64_f8f6f4 v[2:17], v[58:65], v[210:217], v[2:17], v250, v250 op_sel_hi:[0,0,0]
	v_mfma_scale_f32_32x32x64_f8f6f4 v[2:17], v[66:73], v[218:225], v[2:17], v250, v250 op_sel_hi:[0,0,0]
	v_mfma_scale_f32_32x32x64_f8f6f4 v[2:17], v[74:81], v[226:233], v[2:17], v250, v250 op_sel_hi:[0,0,0]
	v_mfma_scale_f32_32x32x64_f8f6f4 v[2:17], v[82:89], v[234:241], v[2:17], v250, v250 op_sel_hi:[0,0,0]
	s_nop 15
	s_nop 3
	v_min3_f32 v2, v2, v3, v4
	v_min3_f32 v5, v5, v6, v7
	v_min3_f32 v8, v8, v9, v10
	v_min3_f32 v11, v11, v12, v13
	v_min3_f32 v14, v14, v15, v16
	v_min3_f32 v2, v2, v5, v8
	v_min3_f32 v11, v11, v14, v17
	v_min3_f32 v251, v251, v2, v11
	ds_bpermute_b32 v3, v248, v251
	s_waitcnt lgkmcnt(0)
	v_min_f32_e32 v2, v251, v3
	ds_write_b32 v249, v2 offset:48128
	global_load_dwordx4 v[194:197], v242, s[22:23] offset:0 nt
	global_load_dwordx4 v[198:201], v242, s[22:23] offset:128 nt
	global_load_dwordx4 v[202:205], v242, s[22:23] offset:256 nt
	global_load_dwordx4 v[206:209], v242, s[22:23] offset:384 nt
	s_waitcnt vmcnt(4)
	v_mul_f32_e32 v6, v178, v178
	v_mul_f32_e32 v7, v182, v182
	v_cvt_pk_fp8_f32 v2, v178, v179
	v_cvt_pk_fp8_f32 v3, v182, v183
	v_cvt_pk_fp8_f32 v4, v186, v187
	v_cvt_pk_fp8_f32 v5, v190, v191
	v_fmac_f32_e32 v6, v179, v179
	v_fmac_f32_e32 v7, v183, v183
	v_fmac_f32_e32 v6, v180, v180
	v_fmac_f32_e32 v7, v184, v184
	v_fmac_f32_e32 v6, v181, v181
	v_fmac_f32_e32 v7, v185, v185
	v_fmac_f32_e32 v6, v186, v186
	v_fmac_f32_e32 v7, v190, v190
	v_fmac_f32_e32 v6, v187, v187
	v_fmac_f32_e32 v7, v191, v191
	v_fmac_f32_e32 v6, v188, v188
	v_fmac_f32_e32 v7, v192, v192
	v_fmac_f32_e32 v6, v189, v189
	v_fmac_f32_e32 v7, v193, v193
	v_cvt_pk_fp8_f32 v2, v180, v181 op_sel:[0,0,1]
	v_cvt_pk_fp8_f32 v3, v184, v185 op_sel:[0,0,1]
	v_cvt_pk_fp8_f32 v4, v188, v189 op_sel:[0,0,1]
	v_cvt_pk_fp8_f32 v5, v192, v193 op_sel:[0,0,1]
	v_add_f32_e32 v6, v6, v7
	s_nop 0
	ds_write_b128 v244, v[2:5] offset:17408
	ds_write_b32 v245, v6 offset:43008
	s_waitcnt lgkmcnt(0)
	s_barrier
	ds_read_b128 v[210:213], v246 offset:17408
	ds_read_b128 v[214:217], v246 offset:17424
	ds_read_b128 v[2:5], v247 offset:34816
	ds_read_b128 v[6:9], v247 offset:34848
	ds_read_b128 v[10:13], v247 offset:34880
	ds_read_b128 v[14:17], v247 offset:34912
	ds_read_b128 v[218:221], v246 offset:17472
	ds_read_b128 v[222:225], v246 offset:17488
	ds_read_b128 v[226:229], v246 offset:17536
	ds_read_b128 v[230:233], v246 offset:17552
	ds_read_b128 v[234:237], v246 offset:17600
	ds_read_b128 v[238:241], v246 offset:17616
	s_waitcnt lgkmcnt(6)
	v_mfma_scale_f32_32x32x64_f8f6f4 v[2:17], v[34:41], v[210:217], v[2:17], v250, v250 op_sel_hi:[0,0,0]
	s_waitcnt lgkmcnt(4)
	v_mfma_scale_f32_32x32x64_f8f6f4 v[2:17], v[26:33], v[218:225], v[2:17], v250, v250 op_sel_hi:[0,0,0]
	s_waitcnt lgkmcnt(2)
	v_mfma_scale_f32_32x32x64_f8f6f4 v[2:17], v[50:57], v[226:233], v[2:17], v250, v250 op_sel_hi:[0,0,0]
	s_waitcnt lgkmcnt(0)
	v_mfma_scale_f32_32x32x64_f8f6f4 v[2:17], v[42:49], v[234:241], v[2:17], v250, v250 op_sel_hi:[0,0,0]
	s_nop 15
	s_nop 3
	v_min3_f32 v2, v2, v3, v4
	v_min3_f32 v5, v5, v6, v7
	v_min3_f32 v8, v8, v9, v10
	v_min3_f32 v11, v11, v12, v13
	v_min3_f32 v14, v14, v15, v16
	v_min3_f32 v2, v2, v5, v8
	v_min3_f32 v11, v11, v14, v17
	v_min_f32_e32 v251, v2, v11
	ds_read_b128 v[2:5], v247 offset:34944
	ds_read_b128 v[6:9], v247 offset:34976
	ds_read_b128 v[10:13], v247 offset:35008
	ds_read_b128 v[14:17], v247 offset:35040
	s_waitcnt lgkmcnt(0)
	v_mfma_scale_f32_32x32x64_f8f6f4 v[2:17], v[18:25], v[210:217], v[2:17], v250, v250 op_sel_hi:[0,0,0]
	v_mfma_scale_f32_32x32x64_f8f6f4 v[2:17], v[130:137], v[218:225], v[2:17], v250, v250 op_sel_hi:[0,0,0]
	v_mfma_scale_f32_32x32x64_f8f6f4 v[2:17], v[122:129], v[226:233], v[2:17], v250, v250 op_sel_hi:[0,0,0]
	v_mfma_scale_f32_32x32x64_f8f6f4 v[2:17], v[138:145], v[234:241], v[2:17], v250, v250 op_sel_hi:[0,0,0]
	s_nop 15
	s_nop 3
	v_min3_f32 v2, v2, v3, v4
	v_min3_f32 v5, v5, v6, v7
	v_min3_f32 v8, v8, v9, v10
	v_min3_f32 v11, v11, v12, v13
	v_min3_f32 v14, v14, v15, v16
	v_min3_f32 v2, v2, v5, v8
	v_min3_f32 v11, v11, v14, v17
	v_min3_f32 v251, v251, v2, v11
	ds_read_b128 v[2:5], v247 offset:35072
	ds_read_b128 v[6:9], v247 offset:35104
	ds_read_b128 v[10:13], v247 offset:35136
	ds_read_b128 v[14:17], v247 offset:35168
	s_waitcnt lgkmcnt(0)
	v_mfma_scale_f32_32x32x64_f8f6f4 v[2:17], v[98:105], v[210:217], v[2:17], v250, v250 op_sel_hi:[0,0,0]
	v_mfma_scale_f32_32x32x64_f8f6f4 v[2:17], v[90:97], v[218:225], v[2:17], v250, v250 op_sel_hi:[0,0,0]
	v_mfma_scale_f32_32x32x64_f8f6f4 v[2:17], v[114:121], v[226:233], v[2:17], v250, v250 op_sel_hi:[0,0,0]
	v_mfma_scale_f32_32x32x64_f8f6f4 v[2:17], v[106:113], v[234:241], v[2:17], v250, v250 op_sel_hi:[0,0,0]
	s_nop 15
	s_nop 3
	v_min3_f32 v2, v2, v3, v4
	v_min3_f32 v5, v5, v6, v7
	v_min3_f32 v8, v8, v9, v10
	v_min3_f32 v11, v11, v12, v13
	v_min3_f32 v14, v14, v15, v16
	v_min3_f32 v2, v2, v5, v8
	v_min3_f32 v11, v11, v14, v17
	v_min3_f32 v251, v251, v2, v11
	ds_read_b128 v[2:5], v247 offset:35200
	ds_read_b128 v[6:9], v247 offset:35232
	ds_read_b128 v[10:13], v247 offset:35264
	ds_read_b128 v[14:17], v247 offset:35296
	s_waitcnt lgkmcnt(0)
	v_mfma_scale_f32_32x32x64_f8f6f4 v[2:17], v[58:65], v[210:217], v[2:17], v250, v250 op_sel_hi:[0,0,0]
	v_mfma_scale_f32_32x32x64_f8f6f4 v[2:17], v[66:73], v[218:225], v[2:17], v250, v250 op_sel_hi:[0,0,0]
	v_mfma_scale_f32_32x32x64_f8f6f4 v[2:17], v[74:81], v[226:233], v[2:17], v250, v250 op_sel_hi:[0,0,0]
	v_mfma_scale_f32_32x32x64_f8f6f4 v[2:17], v[82:89], v[234:241], v[2:17], v250, v250 op_sel_hi:[0,0,0]
	s_nop 15
	s_nop 3
	v_min3_f32 v2, v2, v3, v4
	v_min3_f32 v5, v5, v6, v7
	v_min3_f32 v8, v8, v9, v10
	v_min3_f32 v11, v11, v12, v13
	v_min3_f32 v14, v14, v15, v16
	v_min3_f32 v2, v2, v5, v8
	v_min3_f32 v11, v11, v14, v17
	v_min3_f32 v251, v251, v2, v11
	ds_bpermute_b32 v3, v248, v251
	s_waitcnt lgkmcnt(0)
	v_min_f32_e32 v2, v251, v3
	ds_write_b32 v249, v2 offset:49152
	s_waitcnt vmcnt(0)
	v_mul_f32_e32 v6, v194, v194
	v_mul_f32_e32 v7, v198, v198
	v_cvt_pk_fp8_f32 v2, v194, v195
	v_cvt_pk_fp8_f32 v3, v198, v199
	v_cvt_pk_fp8_f32 v4, v202, v203
	v_cvt_pk_fp8_f32 v5, v206, v207
	v_fmac_f32_e32 v6, v195, v195
	v_fmac_f32_e32 v7, v199, v199
	v_fmac_f32_e32 v6, v196, v196
	v_fmac_f32_e32 v7, v200, v200
	v_fmac_f32_e32 v6, v197, v197
	v_fmac_f32_e32 v7, v201, v201
	v_fmac_f32_e32 v6, v202, v202
	v_fmac_f32_e32 v7, v206, v206
	v_fmac_f32_e32 v6, v203, v203
	v_fmac_f32_e32 v7, v207, v207
	v_fmac_f32_e32 v6, v204, v204
	v_fmac_f32_e32 v7, v208, v208
	v_fmac_f32_e32 v6, v205, v205
	v_fmac_f32_e32 v7, v209, v209
	v_cvt_pk_fp8_f32 v2, v196, v197 op_sel:[0,0,1]
	v_cvt_pk_fp8_f32 v3, v200, v201 op_sel:[0,0,1]
	v_cvt_pk_fp8_f32 v4, v204, v205 op_sel:[0,0,1]
	v_cvt_pk_fp8_f32 v5, v208, v209 op_sel:[0,0,1]
	v_add_f32_e32 v6, v6, v7
	s_nop 0
	ds_write_b128 v244, v[2:5] offset:26112
	ds_write_b32 v245, v6 offset:45056
	s_waitcnt lgkmcnt(0)
	s_barrier
	ds_read_b128 v[210:213], v246 offset:26112
	ds_read_b128 v[214:217], v246 offset:26128
	ds_read_b128 v[2:5], v247 offset:34816
	ds_read_b128 v[6:9], v247 offset:34848
	ds_read_b128 v[10:13], v247 offset:34880
	ds_read_b128 v[14:17], v247 offset:34912
	ds_read_b128 v[218:221], v246 offset:26176
	ds_read_b128 v[222:225], v246 offset:26192
	ds_read_b128 v[226:229], v246 offset:26240
	ds_read_b128 v[230:233], v246 offset:26256
	ds_read_b128 v[234:237], v246 offset:26304
	ds_read_b128 v[238:241], v246 offset:26320
	s_waitcnt lgkmcnt(6)
	v_mfma_scale_f32_32x32x64_f8f6f4 v[2:17], v[34:41], v[210:217], v[2:17], v250, v250 op_sel_hi:[0,0,0]
	s_waitcnt lgkmcnt(4)
	v_mfma_scale_f32_32x32x64_f8f6f4 v[2:17], v[26:33], v[218:225], v[2:17], v250, v250 op_sel_hi:[0,0,0]
	s_waitcnt lgkmcnt(2)
	v_mfma_scale_f32_32x32x64_f8f6f4 v[2:17], v[50:57], v[226:233], v[2:17], v250, v250 op_sel_hi:[0,0,0]
	s_waitcnt lgkmcnt(0)
	v_mfma_scale_f32_32x32x64_f8f6f4 v[2:17], v[42:49], v[234:241], v[2:17], v250, v250 op_sel_hi:[0,0,0]
	s_nop 15
	s_nop 3
	v_min3_f32 v2, v2, v3, v4
	v_min3_f32 v5, v5, v6, v7
	v_min3_f32 v8, v8, v9, v10
	v_min3_f32 v11, v11, v12, v13
	v_min3_f32 v14, v14, v15, v16
	v_min3_f32 v2, v2, v5, v8
	v_min3_f32 v11, v11, v14, v17
	v_min_f32_e32 v251, v2, v11
	ds_read_b128 v[2:5], v247 offset:34944
	ds_read_b128 v[6:9], v247 offset:34976
	ds_read_b128 v[10:13], v247 offset:35008
	ds_read_b128 v[14:17], v247 offset:35040
	s_waitcnt lgkmcnt(0)
	v_mfma_scale_f32_32x32x64_f8f6f4 v[2:17], v[18:25], v[210:217], v[2:17], v250, v250 op_sel_hi:[0,0,0]
	v_mfma_scale_f32_32x32x64_f8f6f4 v[2:17], v[130:137], v[218:225], v[2:17], v250, v250 op_sel_hi:[0,0,0]
	v_mfma_scale_f32_32x32x64_f8f6f4 v[2:17], v[122:129], v[226:233], v[2:17], v250, v250 op_sel_hi:[0,0,0]
	v_mfma_scale_f32_32x32x64_f8f6f4 v[2:17], v[138:145], v[234:241], v[2:17], v250, v250 op_sel_hi:[0,0,0]
	s_nop 15
	s_nop 3
	v_min3_f32 v2, v2, v3, v4
	v_min3_f32 v5, v5, v6, v7
	v_min3_f32 v8, v8, v9, v10
	v_min3_f32 v11, v11, v12, v13
	v_min3_f32 v14, v14, v15, v16
	v_min3_f32 v2, v2, v5, v8
	v_min3_f32 v11, v11, v14, v17
	v_min3_f32 v251, v251, v2, v11
	ds_read_b128 v[2:5], v247 offset:35072
	ds_read_b128 v[6:9], v247 offset:35104
	ds_read_b128 v[10:13], v247 offset:35136
	ds_read_b128 v[14:17], v247 offset:35168
	s_waitcnt lgkmcnt(0)
	v_mfma_scale_f32_32x32x64_f8f6f4 v[2:17], v[98:105], v[210:217], v[2:17], v250, v250 op_sel_hi:[0,0,0]
	v_mfma_scale_f32_32x32x64_f8f6f4 v[2:17], v[90:97], v[218:225], v[2:17], v250, v250 op_sel_hi:[0,0,0]
	v_mfma_scale_f32_32x32x64_f8f6f4 v[2:17], v[114:121], v[226:233], v[2:17], v250, v250 op_sel_hi:[0,0,0]
	v_mfma_scale_f32_32x32x64_f8f6f4 v[2:17], v[106:113], v[234:241], v[2:17], v250, v250 op_sel_hi:[0,0,0]
	s_nop 15
	s_nop 3
	v_min3_f32 v2, v2, v3, v4
	v_min3_f32 v5, v5, v6, v7
	v_min3_f32 v8, v8, v9, v10
	v_min3_f32 v11, v11, v12, v13
	v_min3_f32 v14, v14, v15, v16
	v_min3_f32 v2, v2, v5, v8
	v_min3_f32 v11, v11, v14, v17
	v_min3_f32 v251, v251, v2, v11
	ds_read_b128 v[2:5], v247 offset:35200
	ds_read_b128 v[6:9], v247 offset:35232
	ds_read_b128 v[10:13], v247 offset:35264
	ds_read_b128 v[14:17], v247 offset:35296
	s_waitcnt lgkmcnt(0)
	v_mfma_scale_f32_32x32x64_f8f6f4 v[2:17], v[58:65], v[210:217], v[2:17], v250, v250 op_sel_hi:[0,0,0]
	v_mfma_scale_f32_32x32x64_f8f6f4 v[2:17], v[66:73], v[218:225], v[2:17], v250, v250 op_sel_hi:[0,0,0]
	v_mfma_scale_f32_32x32x64_f8f6f4 v[2:17], v[74:81], v[226:233], v[2:17], v250, v250 op_sel_hi:[0,0,0]
	v_mfma_scale_f32_32x32x64_f8f6f4 v[2:17], v[82:89], v[234:241], v[2:17], v250, v250 op_sel_hi:[0,0,0]
	s_nop 15
	s_nop 3
	v_min3_f32 v2, v2, v3, v4
	v_min3_f32 v5, v5, v6, v7
	v_min3_f32 v8, v8, v9, v10
	v_min3_f32 v11, v11, v12, v13
	v_min3_f32 v14, v14, v15, v16
	v_min3_f32 v2, v2, v5, v8
	v_min3_f32 v11, v11, v14, v17
	v_min3_f32 v251, v251, v2, v11
	ds_bpermute_b32 v3, v248, v251
	s_waitcnt lgkmcnt(0)
	v_min_f32_e32 v2, v251, v3
	ds_write_b32 v249, v2 offset:50176
	v_and_b32_e32 v182, 63, v0
	v_lshlrev_b32_e32 v183, 5, v0
	v_and_b32_e32 v184, 31, v0
	v_and_b32_e32 v185, 63, v0
	v_mov_b32_e32 v186, 64
	v_mov_b32_e32 v187, v248
	s_movk_i32 s2, 0x80
	v_cmp_gt_u32_e32 vcc, s2, v0
	v_mov_b32_e32 v2, 0
	s_waitcnt lgkmcnt(0)
	s_barrier
	s_and_saveexec_b64 s[4:5], vcc
	s_cbranch_execz .LBB1_10
	v_lshlrev_b32_e32 v2, 2, v184
	s_movk_i32 s2, 0xc00
	v_and_or_b32 v2, v183, s2, v2
	v_add_u32_e32 v8, 0xb800, v2
	ds_read2_b32 v[2:3], v8 offset1:32
	ds_read2_b32 v[4:5], v8 offset0:64 offset1:96
	ds_read2_b32 v[6:7], v8 offset0:192 offset1:224
	v_lshlrev_b32_e32 v14, 6, v0
	s_mov_b32 s2, 0xf800000
	s_waitcnt lgkmcnt(2)
	v_max_f32_e32 v3, v3, v3
	v_max_f32_e32 v2, v2, v2
	v_min_f32_e32 v10, v2, v3
	ds_read2_b32 v[2:3], v8 offset0:128 offset1:160
	s_waitcnt lgkmcnt(2)
	v_max_f32_e32 v5, v5, v5
	v_max_f32_e32 v4, v4, v4
	v_min_f32_e32 v11, v4, v5
	s_waitcnt lgkmcnt(1)
	v_max_f32_e32 v4, v7, v7
	v_max_f32_e32 v5, v6, v6
	v_min_f32_e32 v4, v5, v4
	s_waitcnt lgkmcnt(0)
	v_min3_f32 v12, v2, v3, v4
	ds_read_b128 v[2:5], v14 offset:38912
	ds_read_b128 v[6:9], v14 offset:38944
	v_min3_f32 v20, v10, v11, v12
	ds_read_b128 v[10:13], v14 offset:38928
	ds_read_b128 v[14:17], v14 offset:38960
	s_waitcnt lgkmcnt(3)
	v_mov_b32_e32 v18, v2
	s_waitcnt lgkmcnt(2)
	v_mov_b32_e32 v19, v6
	v_mov_b32_e32 v6, v3
	v_pk_add_f32 v[2:3], v[18:19], v[6:7]
	v_mov_b32_e32 v6, v4
	v_mov_b32_e32 v7, v8
	v_mov_b32_e32 v8, v5
	v_pk_add_f32 v[4:5], v[6:7], v[8:9]
	s_waitcnt lgkmcnt(1)
	v_mov_b32_e32 v6, v12
	v_pk_add_f32 v[2:3], v[2:3], v[4:5]
	v_mov_b32_e32 v4, v10
	s_waitcnt lgkmcnt(0)
	v_mov_b32_e32 v5, v14
	v_mov_b32_e32 v14, v11
	v_mov_b32_e32 v7, v16
	v_mov_b32_e32 v16, v13
	v_pk_add_f32 v[4:5], v[4:5], v[14:15]
	v_pk_add_f32 v[6:7], v[6:7], v[16:17]
	s_nop 0
	v_pk_add_f32 v[4:5], v[4:5], v[6:7]
	s_nop 0
	v_pk_add_f32 v[2:3], v[2:3], v[4:5]
	s_nop 0
	v_add_f32_e32 v2, v2, v3
	v_add_f32_e32 v2, v20, v2
	v_max_f32_e32 v2, 0, v2
	v_mul_f32_e32 v3, 0x4f800000, v2
	v_cmp_gt_f32_e32 vcc, s2, v2
	s_nop 1
	v_cndmask_b32_e32 v2, v2, v3, vcc
	v_sqrt_f32_e32 v3, v2
	s_nop 0
	v_add_u32_e32 v4, -1, v3
	v_fma_f32 v5, -v4, v3, v2
	v_cmp_ge_f32_e64 s[2:3], 0, v5
	v_add_u32_e32 v5, 1, v3
	s_nop 0
	v_cndmask_b32_e64 v4, v3, v4, s[2:3]
	v_fma_f32 v3, -v5, v3, v2
	v_cmp_lt_f32_e64 s[2:3], 0, v3
	s_nop 1
	v_cndmask_b32_e64 v3, v4, v5, s[2:3]
	v_mul_f32_e32 v4, 0x37800000, v3
	v_cndmask_b32_e32 v3, v3, v4, vcc
	v_mov_b32_e32 v4, 0x260
	v_cmp_class_f32_e32 vcc, v2, v4
	s_nop 1
	v_cndmask_b32_e32 v2, v3, v2, vcc

.LBB1_12:
	s_or_b64 exec, exec, s[2:3]
	v_cmp_eq_u32_e32 vcc, 0, v0
	s_waitcnt lgkmcnt(0)
	s_barrier
	s_and_saveexec_b64 s[2:3], vcc
	s_cbranch_execz .LBB1_15
	s_mov_b64 s[2:3], exec
	v_mbcnt_lo_u32_b32 v0, s2, 0
	v_mbcnt_hi_u32_b32 v0, s3, v0
	v_cmp_eq_u32_e32 vcc, 0, v0
	s_and_b64 s[4:5], exec, vcc
	s_mov_b64 exec, s[4:5]
	s_cbranch_execz .LBB1_15
	v_mov_b32_e32 v4, 0
	ds_read_b128 v[0:3], v4 offset:51200
	s_load_dwordx2 s[0:1], s[0:1], 0x18
	s_lshr_b32 s2, s30, 4
	s_lshl_b32 s2, s2, 7
	s_add_u32 s2, s2, 0x300000
	s_add_u32 s6, s6, s2
	s_addc_u32 s7, s7, 0
	s_mov_b32 s4, 0
	s_mov_b32 s5, 0x41d00000
	s_mov_b32 s8, 0
	s_mov_b32 s9, 0x420e0000
	s_waitcnt lgkmcnt(0)
	v_add_f32_e32 v0, v0, v1
	v_add_f32_e32 v1, v2, v3
	v_add_f32_e32 v0, v0, v1
	v_cvt_f64_f32_e32 v[6:7], v0
	v_add_f64 v[8:9], v[6:7], s[4:5]
	global_atomic_add_f64 v[10:11], v4, v[8:9], s[6:7] sc0
	s_waitcnt vmcnt(0)
	v_cmp_le_f64_e32 vcc, s[8:9], v[10:11]
	s_and_saveexec_b64 s[2:3], vcc
	s_cbranch_execz .LBB1_15
	v_add_f64 v[10:11], v[10:11], -s[8:9]
	v_add_f64 v[10:11], v[10:11], v[6:7]
	v_cvt_f32_f64_e32 v0, v[10:11]
	v_mul_f32_e32 v0, 0x38000000, v0
	global_atomic_add_f32 v4, v0, s[0:1]

amdhsa.kernels:
  - .agpr_count:     0
    .args:
      - .actual_access:  read_only
        .address_space:  global
        .offset:         0
        .size:           8
        .value_kind:     global_buffer
      - .actual_access:  write_only
        .address_space:  global
        .offset:         8
        .size:           8
        .value_kind:     global_buffer
      - .actual_access:  write_only
        .address_space:  global
        .offset:         16
        .size:           8
        .value_kind:     global_buffer
      - .actual_access:  write_only
        .address_space:  global
        .offset:         24
        .size:           8
        .value_kind:     global_buffer
    .group_segment_fixed_size: 8704
    .kernarg_segment_align: 8
    .kernarg_segment_size: 32
    .language:       OpenCL C
    .language_version:
      - 2
      - 0
    .max_flat_workgroup_size: 64
    .name:           _Z11center_prepPKfPcPfS2_
    .private_segment_fixed_size: 0
    .sgpr_count:     18
    .sgpr_spill_count: 0
    .symbol:         _Z11center_prepPKfPcPfS2_.kd
    .uniform_work_group_size: 1
    .uses_dynamic_stack: false
    .vgpr_count:     164
    .vgpr_spill_count: 0
    .wavefront_size: 64
  - .agpr_count:     0
    .args:
      - .actual_access:  read_only
        .address_space:  global
        .offset:         0
        .size:           8
        .value_kind:     global_buffer
      - .actual_access:  read_only
        .address_space:  global
        .offset:         8
        .size:           8
        .value_kind:     global_buffer
      - .actual_access:  read_only
        .address_space:  global
        .offset:         16
        .size:           8
        .value_kind:     global_buffer
      - .address_space:  global
        .offset:         24
        .size:           8
        .value_kind:     global_buffer
    .group_segment_fixed_size: 51232
    .kernarg_segment_align: 8
    .kernarg_segment_size: 32
    .language:       OpenCL C
    .language_version:
      - 2
      - 0
    .max_flat_workgroup_size: 512
    .name:           _Z11center_mainPKfPKcS0_Pf
    .private_segment_fixed_size: 0
    .sgpr_count:     18
    .sgpr_spill_count: 0
    .symbol:         _Z11center_mainPKfPKcS0_Pf.kd
    .uniform_work_group_size: 1
    .uses_dynamic_stack: false
    .vgpr_count:     256
    .vgpr_spill_count: 0
    .wavefront_size: 64
